# k_tri actF stores nt; attention loop: removed redundant S-copy v_mov_b64 and ones-reg movs (read tile regs directly)
# speedup vs baseline: 1.0159x; 1.0143x over previous
.LBB0_17:
	s_or_b64 exec, exec, s[0:1]
	s_waitcnt lgkmcnt(0)
	v_add_f32_e32 v132, v154, v218
	s_waitcnt vmcnt(32)
	v_mov_b32_e32 v133, 0x3727c5ac
	v_fmac_f32_e32 v133, 0x3c000000, v132
	s_mov_b32 s0, 0x800000
	v_mul_f32_e32 v132, 0x4b800000, v133
	v_cmp_gt_f32_e32 vcc, s0, v133
	v_lshlrev_b32_e32 v154, 4, v216
	s_movk_i32 s0, 0x1000
	v_cndmask_b32_e32 v132, v133, v132, vcc
	v_rsq_f32_e32 v132, v132
	s_nop 0
	v_mul_f32_e32 v133, 0x45800000, v132
	v_cndmask_b32_e32 v132, v132, v133, vcc
	v_pk_mul_f32 v[134:135], v[134:135], v[132:133] op_sel_hi:[1,0]
	s_waitcnt vmcnt(28)
	v_pk_fma_f32 v[10:11], v[134:135], v[10:11], v[14:15]
	v_pk_mul_f32 v[14:15], v[136:137], v[132:133] op_sel_hi:[1,0]
	v_cvt_pk_f16_f32 v10, v10, v11
	v_pk_fma_f32 v[12:13], v[14:15], v[12:13], v[16:17]
	v_pk_mul_f32 v[14:15], v[158:159], v[132:133] op_sel_hi:[1,0]
	v_cvt_pk_f16_f32 v11, v12, v13
	v_pk_mul_f32 v[12:13], v[138:139], v[132:133] op_sel_hi:[1,0]
	s_waitcnt vmcnt(22)
	v_pk_fma_f32 v[14:15], v[14:15], v[36:37], v[40:41]
	v_pk_fma_f32 v[2:3], v[12:13], v[2:3], v[6:7]
	v_pk_mul_f32 v[6:7], v[148:149], v[132:133] op_sel_hi:[1,0]
	v_cvt_pk_f16_f32 v12, v2, v3
	v_pk_mul_f32 v[2:3], v[140:141], v[132:133] op_sel_hi:[1,0]
	v_pk_fma_f32 v[6:7], v[6:7], v[20:21], v[24:25]
	v_pk_fma_f32 v[2:3], v[2:3], v[4:5], v[8:9]
	v_pk_mul_f32 v[4:5], v[144:145], v[132:133] op_sel_hi:[1,0]
	v_cvt_pk_f16_f32 v13, v2, v3
	v_pk_mul_f32 v[2:3], v[142:143], v[132:133] op_sel_hi:[1,0]
	v_pk_fma_f32 v[4:5], v[4:5], v[28:29], v[32:33]
	v_pk_fma_f32 v[2:3], v[2:3], v[26:27], v[30:31]
	v_pk_mul_f32 v[8:9], v[152:153], v[132:133] op_sel_hi:[1,0]
	v_cvt_pk_f16_f32 v2, v2, v3
	v_cvt_pk_f16_f32 v3, v4, v5
	v_pk_mul_f32 v[4:5], v[146:147], v[132:133] op_sel_hi:[1,0]
	s_waitcnt vmcnt(20)
	v_pk_fma_f32 v[8:9], v[8:9], v[44:45], v[48:49]
	v_pk_fma_f32 v[4:5], v[4:5], v[18:19], v[22:23]
	v_pk_mul_f32 v[16:17], v[162:163], v[132:133] op_sel_hi:[1,0]
	v_cvt_pk_f16_f32 v4, v4, v5
	v_cvt_pk_f16_f32 v5, v6, v7
	v_pk_mul_f32 v[6:7], v[150:151], v[132:133] op_sel_hi:[1,0]
	s_waitcnt vmcnt(16)
	v_pk_fma_f32 v[16:17], v[16:17], v[124:125], v[128:129]
	v_pk_fma_f32 v[6:7], v[6:7], v[42:43], v[46:47]
	v_pk_mul_f32 v[18:19], v[166:167], v[132:133] op_sel_hi:[1,0]
	v_cvt_pk_f16_f32 v6, v6, v7
	v_cvt_pk_f16_f32 v7, v8, v9
	v_pk_mul_f32 v[8:9], v[156:157], v[132:133] op_sel_hi:[1,0]
	v_pk_fma_f32 v[18:19], v[18:19], v[108:109], v[116:117]
	v_pk_fma_f32 v[8:9], v[8:9], v[34:35], v[38:39]
	v_pk_mul_f32 v[20:21], v[170:171], v[132:133] op_sel_hi:[1,0]
	v_cvt_pk_f16_f32 v8, v8, v9
	v_cvt_pk_f16_f32 v9, v14, v15
	v_pk_mul_f32 v[14:15], v[160:161], v[132:133] op_sel_hi:[1,0]
	s_waitcnt vmcnt(12)
	v_pk_fma_f32 v[20:21], v[20:21], v[112:113], v[120:121]
	v_pk_fma_f32 v[14:15], v[14:15], v[122:123], v[126:127]
	v_pk_mul_f32 v[22:23], v[174:175], v[132:133] op_sel_hi:[1,0]
	v_cvt_pk_f16_f32 v14, v14, v15
	v_cvt_pk_f16_f32 v15, v16, v17
	v_pk_mul_f32 v[16:17], v[164:165], v[132:133] op_sel_hi:[1,0]
	v_pk_fma_f32 v[22:23], v[22:23], v[92:93], v[100:101]
	v_pk_fma_f32 v[16:17], v[16:17], v[106:107], v[114:115]
	v_pk_mul_f32 v[24:25], v[178:179], v[132:133] op_sel_hi:[1,0]
	v_cvt_pk_f16_f32 v16, v16, v17
	v_cvt_pk_f16_f32 v17, v18, v19
	v_pk_mul_f32 v[18:19], v[168:169], v[132:133] op_sel_hi:[1,0]
	s_waitcnt vmcnt(8)
	v_pk_fma_f32 v[24:25], v[24:25], v[96:97], v[104:105]
	v_pk_fma_f32 v[18:19], v[18:19], v[110:111], v[118:119]
	v_pk_mul_f32 v[26:27], v[196:197], v[132:133] op_sel_hi:[1,0]
	v_cvt_pk_f16_f32 v18, v18, v19
	v_cvt_pk_f16_f32 v19, v20, v21
	v_pk_mul_f32 v[20:21], v[172:173], v[132:133] op_sel_hi:[1,0]
	v_pk_fma_f32 v[26:27], v[26:27], v[76:77], v[84:85]
	v_pk_fma_f32 v[20:21], v[20:21], v[90:91], v[98:99]
	v_pk_mul_f32 v[28:29], v[192:193], v[132:133] op_sel_hi:[1,0]
	v_cvt_pk_f16_f32 v20, v20, v21
	v_cvt_pk_f16_f32 v21, v22, v23
	v_pk_mul_f32 v[22:23], v[176:177], v[132:133] op_sel_hi:[1,0]
	s_waitcnt vmcnt(4)
	v_pk_fma_f32 v[28:29], v[28:29], v[80:81], v[88:89]
	v_pk_fma_f32 v[22:23], v[22:23], v[94:95], v[102:103]
	v_pk_mul_f32 v[30:31], v[188:189], v[132:133] op_sel_hi:[1,0]
	v_cvt_pk_f16_f32 v22, v22, v23
	v_cvt_pk_f16_f32 v23, v24, v25
	v_pk_mul_f32 v[24:25], v[198:199], v[132:133] op_sel_hi:[1,0]
	v_pk_fma_f32 v[30:31], v[30:31], v[60:61], v[68:69]
	v_pk_fma_f32 v[24:25], v[24:25], v[74:75], v[82:83]
	v_pk_mul_f32 v[32:33], v[184:185], v[132:133] op_sel_hi:[1,0]
	v_cvt_pk_f16_f32 v24, v24, v25
	v_cvt_pk_f16_f32 v25, v26, v27
	v_pk_mul_f32 v[26:27], v[194:195], v[132:133] op_sel_hi:[1,0]
	s_waitcnt vmcnt(0)
	v_pk_fma_f32 v[32:33], v[32:33], v[64:65], v[72:73]
	v_pk_fma_f32 v[26:27], v[26:27], v[78:79], v[86:87]
	v_pk_mul_f32 v[34:35], v[180:181], v[132:133] op_sel_hi:[1,0]
	v_cvt_pk_f16_f32 v26, v26, v27
	v_cvt_pk_f16_f32 v27, v28, v29
	v_pk_mul_f32 v[28:29], v[190:191], v[132:133] op_sel_hi:[1,0]
	v_pk_fma_f32 v[34:35], v[34:35], v[52:53], v[56:57]
	v_pk_fma_f32 v[28:29], v[28:29], v[58:59], v[66:67]
	v_cvt_f16_f32_e32 v36, v214
	v_cvt_pk_f16_f32 v28, v28, v29
	v_cvt_pk_f16_f32 v29, v30, v31
	v_pk_mul_f32 v[30:31], v[186:187], v[132:133] op_sel_hi:[1,0]
	v_cvt_f16_f32_e32 v37, v213
	v_pk_fma_f32 v[30:31], v[30:31], v[62:63], v[70:71]
	v_cvt_f16_f32_e32 v39, v212
	v_cvt_pk_f16_f32 v30, v30, v31
	v_cvt_pk_f16_f32 v31, v32, v33
	v_pk_mul_f32 v[32:33], v[182:183], v[132:133] op_sel_hi:[1,0]
	v_cvt_f16_f32_e32 v41, v209
	v_pk_fma_f32 v[32:33], v[32:33], v[50:51], v[54:55]
	v_cvt_f16_f32_e32 v42, v208
	v_cvt_pk_f16_f32 v32, v32, v33
	v_cvt_pk_f16_f32 v33, v34, v35
	v_lshlrev_b64 v[34:35], 13, v[130:131]
	v_lshl_add_u64 v[34:35], s[14:15], 0, v[34:35]
	v_lshl_add_u64 v[34:35], v[34:35], 0, v[154:155]
	global_store_dwordx4 v[34:35], v[10:13], off nt
	global_store_dwordx4 v[34:35], v[2:5], off offset:1024 nt
	global_store_dwordx4 v[34:35], v[6:9], off offset:2048 nt
	global_store_dwordx4 v[34:35], v[14:17], off offset:3072 nt
	v_add_co_u32_e32 v34, vcc, s0, v34
	v_lshlrev_b32_e32 v38, 4, v0
	s_nop 0
	v_addc_co_u32_e32 v35, vcc, 0, v35, vcc
	global_store_dwordx4 v[34:35], v[18:21], off nt
	global_store_dwordx4 v[34:35], v[22:25], off offset:1024 nt
	global_store_dwordx4 v[34:35], v[26:29], off offset:2048 nt
	global_store_dwordx4 v[34:35], v[30:33], off offset:3072 nt
	v_cvt_f16_f32_e32 v35, v215
	v_and_b32_e32 v34, 28, v0
	v_cmp_eq_u32_e32 vcc, 0, v34
	s_nop 1
	v_cndmask_b32_e32 v34, 0, v35, vcc
	v_cndmask_b32_e32 v40, 0, v36, vcc
	v_cndmask_b32_e32 v35, 0, v37, vcc
	v_cvt_f16_f32_e32 v36, v211
	v_cvt_f16_f32_e32 v37, v210
	v_cndmask_b32_e32 v39, 0, v39, vcc
	v_pack_b32_f16 v35, v35, v39
	v_cndmask_b32_e32 v36, 0, v36, vcc
	v_cndmask_b32_e32 v43, 0, v37, vcc
	v_cndmask_b32_e32 v37, 0, v41, vcc
	v_cndmask_b32_e32 v41, 0, v42, vcc
	v_pack_b32_f16 v37, v37, v41
	v_pack_b32_f16 v36, v36, v43
	v_pack_b32_f16 v34, v34, v40
	ds_write_b128 v38, v[34:37] offset:32768
	v_cvt_f16_f32_e32 v35, v206
	v_cvt_f16_f32_e32 v36, v205
	v_cvt_f16_f32_e32 v37, v204
	v_cvt_f16_f32_e32 v34, v207
	v_cndmask_b32_e32 v39, 0, v35, vcc
	v_cndmask_b32_e32 v35, 0, v36, vcc
	v_cndmask_b32_e32 v40, 0, v37, vcc
	v_cvt_f16_f32_e32 v36, v203
	v_cvt_f16_f32_e32 v37, v202
	v_cvt_f16_f32_e32 v41, v201
	v_cvt_f16_f32_e32 v42, v200
	v_cndmask_b32_e32 v34, 0, v34, vcc
	v_cndmask_b32_e32 v36, 0, v36, vcc
	v_cndmask_b32_e32 v43, 0, v37, vcc
	v_cndmask_b32_e32 v37, 0, v41, vcc
	v_cndmask_b32_e32 v41, 0, v42, vcc
	v_pack_b32_f16 v37, v37, v41
	v_pack_b32_f16 v36, v36, v43
	v_pack_b32_f16 v35, v35, v40
	v_pack_b32_f16 v34, v34, v39
	ds_write_b128 v38, v[34:37] offset:36864
	s_waitcnt lgkmcnt(0)
	s_barrier
	ds_read_b128 v[34:37], v154 offset:32768
	ds_read_b128 v[38:41], v154 offset:33792
	s_waitcnt lgkmcnt(1)
	v_mfma_f32_32x32x16_f16 a[0:15], v[10:13], v[34:37], 0
	v_cmp_gt_u32_e32 vcc, 4, v1
	s_waitcnt lgkmcnt(0)
	v_mfma_f32_32x32x16_f16 a[0:15], v[2:5], v[38:41], a[0:15]
	ds_read_b128 v[2:5], v154 offset:34816
	ds_read_b128 v[10:13], v154 offset:35840
	s_waitcnt lgkmcnt(1)
	v_mfma_f32_32x32x16_f16 a[0:15], v[6:9], v[2:5], a[0:15]
	ds_read_b128 v[2:5], v154 offset:36864
	ds_read_b128 v[6:9], v154 offset:37888
	s_waitcnt lgkmcnt(2)
	v_mfma_f32_32x32x16_f16 a[0:15], v[14:17], v[10:13], a[0:15]
	s_waitcnt lgkmcnt(1)
	v_mfma_f32_32x32x16_f16 a[0:15], v[18:21], v[2:5], a[0:15]
	s_waitcnt lgkmcnt(0)
	v_mfma_f32_32x32x16_f16 a[0:15], v[22:25], v[6:9], a[0:15]
	ds_read_b128 v[2:5], v154 offset:38912
	ds_read_b128 v[6:9], v154 offset:39936
	s_waitcnt lgkmcnt(1)
	v_mfma_f32_32x32x16_f16 a[0:15], v[26:29], v[2:5], a[0:15]
	s_waitcnt lgkmcnt(0)
	v_mfma_f32_32x32x16_f16 a[0:15], v[30:33], v[6:9], a[0:15]
	s_and_saveexec_b64 s[0:1], vcc
	s_cbranch_execz .LBB0_19
	v_ashrrev_i32_e32 v18, 5, v130
	v_and_b32_e32 v18, -8, v18
	v_lshl_add_u32 v1, v1, 6, v18
	v_and_or_b32 v18, v130, 7, v1
	v_ashrrev_i32_e32 v19, 31, v18
	v_lshlrev_b64 v[18:19], 6, v[18:19]
	v_and_b32_e32 v0, 32, v0
	v_bfe_u32 v1, v130, 3, 5
	s_nop 1
	v_accvgpr_read_b32 v17, a15
	v_or3_b32 v18, v18, v0, v1
	v_accvgpr_read_b32 v16, a14
	v_accvgpr_read_b32 v15, a13
	v_accvgpr_read_b32 v14, a12
	v_accvgpr_read_b32 v13, a11
	v_accvgpr_read_b32 v12, a10
	v_accvgpr_read_b32 v11, a9
	v_accvgpr_read_b32 v10, a8
	v_accvgpr_read_b32 v9, a7
	v_accvgpr_read_b32 v8, a6
	v_accvgpr_read_b32 v7, a5
	v_accvgpr_read_b32 v6, a4
	v_accvgpr_read_b32 v5, a3
	v_accvgpr_read_b32 v4, a2
	v_accvgpr_read_b32 v3, a1
	v_accvgpr_read_b32 v2, a0
	v_lshlrev_b64 v[0:1], 5, v[18:19]
	v_lshl_add_u64 v[18:19], s[12:13], 0, v[0:1]
	v_cvt_pk_f16_f32 v9, v8, v9
	v_cvt_pk_f16_f32 v8, v6, v7
	v_cvt_pk_f16_f32 v7, v4, v5
	v_cvt_pk_f16_f32 v6, v2, v3
	v_cvt_pk_f16_f32 v3, v16, v17
	v_cvt_pk_f16_f32 v2, v14, v15
	v_cvt_pk_f16_f32 v1, v12, v13
	v_cvt_pk_f16_f32 v0, v10, v11
	global_store_dwordx4 v[18:19], v[6:9], off
	global_store_dwordx4 v[18:19], v[0:3], off offset:16

.LBB1_6:
	v_mov_b32_e32 v195, v194
	v_mov_b32_e32 v196, v194
	v_mov_b32_e32 v197, v194
	s_setprio 1
	s_and_b64 vcc, exec, s[2:3]
	s_cbranch_vccnz .LBB1_61
	v_cndmask_b32_e64 v1, 0, 1, s[0:1]
	v_cmp_ne_u32_e64 s[16:17], 1, v1
	s_andn2_b64 vcc, exec, s[0:1]
	s_cbranch_vccz .LBB1_62

.LBB1_20:
	v_max_f32_e32 v3, v241, v241
	v_max_f32_e32 v4, v242, v242
	v_max_f32_e32 v3, v4, v3
	v_max_f32_e32 v4, v239, v239
	v_max_f32_e32 v5, v240, v240
	v_max_f32_e32 v4, v5, v4
	v_max_f32_e32 v5, v237, v237
	v_max_f32_e32 v6, v238, v238
	v_max3_f32 v3, v1, v243, v3
	v_max_f32_e32 v5, v6, v5
	v_max3_f32 v3, v3, v4, v5
	v_mov_b32_e32 v4, v3
	s_nop 1
	v_permlane32_swap_b32_e32 v3, v4
	v_max3_f32 v236, v3, v4, s43
	s_setprio 1
	v_sub_f32_e32 v1, v1, v236
	v_cmp_le_f32_e32 vcc, s56, v1
	s_cbranch_vccz .LBB1_82
	ds_read_b128 v[10:13], v206 offset:49152
	v_sub_f32_e32 v1, v66, v236
	v_sub_f32_e32 v3, v68, v236
	v_sub_f32_e32 v5, v70, v236
	v_sub_f32_e32 v7, v72, v236
	v_exp_f32_e32 v14, v1
	v_sub_f32_e32 v1, v67, v236
	v_exp_f32_e32 v4, v3
	v_sub_f32_e32 v3, v69, v236
	v_exp_f32_e32 v6, v5
	v_sub_f32_e32 v5, v71, v236
	v_exp_f32_e32 v8, v7
	v_sub_f32_e32 v7, v73, v236
	v_exp_f32_e32 v7, v7
	v_exp_f32_e32 v5, v5
	v_exp_f32_e32 v3, v3
	v_exp_f32_e32 v1, v1
	v_cvt_pk_f16_f32 v9, v8, v7
	v_cvt_pk_f16_f32 v8, v6, v5
	v_cvt_pk_f16_f32 v7, v4, v3
	v_cvt_pk_f16_f32 v6, v14, v1
	s_waitcnt lgkmcnt(0)
	s_nop 0
	v_mfma_f32_32x32x16_f16 v[98:113], v[10:13], v[6:9], 0
	v_mfma_f32_32x32x16_f16 v[82:97], v[194:197], v[6:9], 0
	v_sub_f32_e32 v1, v243, v236
	v_cmp_le_f32_e32 vcc, s56, v1
	s_cbranch_vccz .LBB1_23
.LBB1_22:
	v_sub_f32_e32 v4, v76, v236
	v_exp_f32_e32 v8, v4
	v_sub_f32_e32 v4, v78, v236
	v_exp_f32_e32 v10, v4
	v_sub_f32_e32 v4, v80, v236
	v_exp_f32_e32 v12, v4
	ds_read_b128 v[4:7], v206 offset:50176
	v_sub_f32_e32 v1, v74, v236
	v_sub_f32_e32 v3, v75, v236
	v_sub_f32_e32 v9, v77, v236
	v_sub_f32_e32 v11, v79, v236
	v_sub_f32_e32 v13, v81, v236
	v_exp_f32_e32 v1, v1
	v_exp_f32_e32 v13, v13
	v_exp_f32_e32 v14, v11
	v_exp_f32_e32 v9, v9
	v_exp_f32_e32 v3, v3
	v_cvt_pk_f16_f32 v11, v12, v13
	v_cvt_pk_f16_f32 v10, v10, v14
	v_cvt_pk_f16_f32 v9, v8, v9
	v_cvt_pk_f16_f32 v8, v1, v3
	s_waitcnt lgkmcnt(0)
	s_nop 0
	v_mfma_f32_32x32x16_f16 v[98:113], v[4:7], v[8:11], v[98:113]
	v_mfma_f32_32x32x16_f16 v[82:97], v[194:197], v[8:11], v[82:97]
.LBB1_23:
	v_sub_f32_e32 v1, v242, v236
	v_cmp_le_f32_e32 vcc, s56, v1
	s_cbranch_vccz .LBB1_83
	ds_read_b128 v[10:13], v206 offset:51200
	v_sub_f32_e32 v1, v50, v236
	v_sub_f32_e32 v3, v52, v236
	v_sub_f32_e32 v5, v54, v236
	v_sub_f32_e32 v7, v56, v236
	v_exp_f32_e32 v14, v1
	v_sub_f32_e32 v1, v51, v236
	v_exp_f32_e32 v4, v3
	v_sub_f32_e32 v3, v53, v236
	v_exp_f32_e32 v6, v5
	v_sub_f32_e32 v5, v55, v236
	v_exp_f32_e32 v8, v7
	v_sub_f32_e32 v7, v57, v236
	v_exp_f32_e32 v7, v7
	v_exp_f32_e32 v5, v5
	v_exp_f32_e32 v3, v3
	v_exp_f32_e32 v1, v1
	v_cvt_pk_f16_f32 v9, v8, v7
	v_cvt_pk_f16_f32 v8, v6, v5
	v_cvt_pk_f16_f32 v7, v4, v3
	v_cvt_pk_f16_f32 v6, v14, v1
	s_waitcnt lgkmcnt(0)
	s_nop 0
	v_mfma_f32_32x32x16_f16 v[98:113], v[10:13], v[6:9], v[98:113]
	v_mfma_f32_32x32x16_f16 v[82:97], v[194:197], v[6:9], v[82:97]
	v_sub_f32_e32 v1, v241, v236
	v_cmp_le_f32_e32 vcc, s56, v1
	s_cbranch_vccz .LBB1_26
.LBB1_25:
	v_sub_f32_e32 v4, v60, v236
	v_exp_f32_e32 v8, v4
	v_sub_f32_e32 v4, v62, v236
	v_exp_f32_e32 v10, v4
	v_sub_f32_e32 v4, v64, v236
	v_exp_f32_e32 v12, v4
	ds_read_b128 v[4:7], v206 offset:52224
	v_sub_f32_e32 v1, v58, v236
	v_sub_f32_e32 v3, v59, v236
	v_sub_f32_e32 v9, v61, v236
	v_sub_f32_e32 v11, v63, v236
	v_sub_f32_e32 v13, v65, v236
	v_exp_f32_e32 v1, v1
	v_exp_f32_e32 v13, v13
	v_exp_f32_e32 v14, v11
	v_exp_f32_e32 v9, v9
	v_exp_f32_e32 v3, v3
	v_cvt_pk_f16_f32 v11, v12, v13
	v_cvt_pk_f16_f32 v10, v10, v14
	v_cvt_pk_f16_f32 v9, v8, v9
	v_cvt_pk_f16_f32 v8, v1, v3
	s_waitcnt lgkmcnt(0)
	s_nop 0
	v_mfma_f32_32x32x16_f16 v[98:113], v[4:7], v[8:11], v[98:113]
	v_mfma_f32_32x32x16_f16 v[82:97], v[194:197], v[8:11], v[82:97]
.LBB1_26:
	v_sub_f32_e32 v1, v240, v236
	v_cmp_le_f32_e32 vcc, s56, v1
	s_cbranch_vccz .LBB1_84
	ds_read_b128 v[10:13], v206 offset:53248
	v_sub_f32_e32 v1, v34, v236
	v_sub_f32_e32 v3, v36, v236
	v_sub_f32_e32 v5, v38, v236
	v_sub_f32_e32 v7, v40, v236
	v_exp_f32_e32 v14, v1
	v_sub_f32_e32 v1, v35, v236
	v_exp_f32_e32 v4, v3
	v_sub_f32_e32 v3, v37, v236
	v_exp_f32_e32 v6, v5
	v_sub_f32_e32 v5, v39, v236
	v_exp_f32_e32 v8, v7
	v_sub_f32_e32 v7, v41, v236
	v_exp_f32_e32 v7, v7
	v_exp_f32_e32 v5, v5
	v_exp_f32_e32 v3, v3
	v_exp_f32_e32 v1, v1
	v_cvt_pk_f16_f32 v9, v8, v7
	v_cvt_pk_f16_f32 v8, v6, v5
	v_cvt_pk_f16_f32 v7, v4, v3
	v_cvt_pk_f16_f32 v6, v14, v1
	s_waitcnt lgkmcnt(0)
	s_nop 0
	v_mfma_f32_32x32x16_f16 v[98:113], v[10:13], v[6:9], v[98:113]
	v_mfma_f32_32x32x16_f16 v[82:97], v[194:197], v[6:9], v[82:97]
	v_sub_f32_e32 v1, v239, v236
	v_cmp_le_f32_e32 vcc, s56, v1
	s_cbranch_vccz .LBB1_29
.LBB1_28:
	v_sub_f32_e32 v4, v44, v236
	v_exp_f32_e32 v8, v4
	v_sub_f32_e32 v4, v46, v236
	v_exp_f32_e32 v10, v4
	v_sub_f32_e32 v4, v48, v236
	v_exp_f32_e32 v12, v4
	ds_read_b128 v[4:7], v206 offset:54272
	v_sub_f32_e32 v1, v42, v236
	v_sub_f32_e32 v3, v43, v236
	v_sub_f32_e32 v9, v45, v236
	v_sub_f32_e32 v11, v47, v236
	v_sub_f32_e32 v13, v49, v236
	v_exp_f32_e32 v1, v1
	v_exp_f32_e32 v13, v13
	v_exp_f32_e32 v14, v11
	v_exp_f32_e32 v9, v9
	v_exp_f32_e32 v3, v3
	v_cvt_pk_f16_f32 v11, v12, v13
	v_cvt_pk_f16_f32 v10, v10, v14
	v_cvt_pk_f16_f32 v9, v8, v9
	v_cvt_pk_f16_f32 v8, v1, v3
	s_waitcnt lgkmcnt(0)
	s_nop 0
	v_mfma_f32_32x32x16_f16 v[98:113], v[4:7], v[8:11], v[98:113]
	v_mfma_f32_32x32x16_f16 v[82:97], v[194:197], v[8:11], v[82:97]
.LBB1_29:
	v_sub_f32_e32 v1, v238, v236
	v_cmp_le_f32_e32 vcc, s56, v1
	s_cbranch_vccz .LBB1_85
	ds_read_b128 v[10:13], v206 offset:55296
	v_sub_f32_e32 v1, v18, v236
	v_sub_f32_e32 v3, v20, v236
	v_sub_f32_e32 v5, v22, v236
	v_sub_f32_e32 v7, v24, v236
	v_exp_f32_e32 v14, v1
	v_sub_f32_e32 v1, v19, v236
	v_exp_f32_e32 v4, v3
	v_sub_f32_e32 v3, v21, v236
	v_exp_f32_e32 v6, v5
	v_sub_f32_e32 v5, v23, v236
	v_exp_f32_e32 v8, v7
	v_sub_f32_e32 v7, v25, v236
	v_exp_f32_e32 v7, v7
	v_exp_f32_e32 v5, v5
	v_exp_f32_e32 v3, v3
	v_exp_f32_e32 v1, v1
	v_cvt_pk_f16_f32 v9, v8, v7
	v_cvt_pk_f16_f32 v8, v6, v5
	v_cvt_pk_f16_f32 v7, v4, v3
	v_cvt_pk_f16_f32 v6, v14, v1
	s_waitcnt lgkmcnt(0)
	s_nop 0
	v_mfma_f32_32x32x16_f16 v[98:113], v[10:13], v[6:9], v[98:113]
	v_mfma_f32_32x32x16_f16 v[82:97], v[194:197], v[6:9], v[82:97]
	v_sub_f32_e32 v1, v237, v236
	v_cmp_le_f32_e32 vcc, s56, v1
	s_cbranch_vccz .LBB1_32
.LBB1_31:
	v_sub_f32_e32 v4, v28, v236
	v_exp_f32_e32 v8, v4
	v_sub_f32_e32 v4, v30, v236
	v_exp_f32_e32 v10, v4
	v_sub_f32_e32 v4, v32, v236
	v_exp_f32_e32 v12, v4
	ds_read_b128 v[4:7], v206 offset:56320
	v_sub_f32_e32 v1, v26, v236
	v_sub_f32_e32 v3, v27, v236
	v_sub_f32_e32 v9, v29, v236
	v_sub_f32_e32 v11, v31, v236
	v_sub_f32_e32 v13, v33, v236
	v_exp_f32_e32 v1, v1
	v_exp_f32_e32 v13, v13
	v_exp_f32_e32 v14, v11
	v_exp_f32_e32 v9, v9
	v_exp_f32_e32 v3, v3
	v_cvt_pk_f16_f32 v11, v12, v13
	v_cvt_pk_f16_f32 v10, v10, v14
	v_cvt_pk_f16_f32 v9, v8, v9
	v_cvt_pk_f16_f32 v8, v1, v3
	s_waitcnt lgkmcnt(0)
	s_nop 0
	v_mfma_f32_32x32x16_f16 v[98:113], v[4:7], v[8:11], v[98:113]
	v_mfma_f32_32x32x16_f16 v[82:97], v[194:197], v[8:11], v[82:97]

.LBB1_47:
	v_max_f32_e32 v3, v14, v14
	v_max_f32_e32 v4, v15, v15
	v_max_f32_e32 v3, v4, v3
	v_max_f32_e32 v4, v12, v12
	v_max_f32_e32 v5, v13, v13
	v_max_f32_e32 v4, v5, v4
	v_max_f32_e32 v5, v9, v9
	v_max_f32_e32 v6, v11, v11
	v_max3_f32 v3, v1, v16, v3
	v_max_f32_e32 v5, v6, v5
	v_max3_f32 v3, v3, v4, v5
	v_mov_b32_e32 v4, v3
	s_nop 1
	v_permlane32_swap_b32_e32 v3, v4
	v_max3_f32 v10, v236, v3, v4
	v_sub_f32_e32 v3, v236, v10
	v_exp_f32_e32 v4, v3
	s_nop 0
	v_mul_f32_e32 v82, v82, v4
	v_pk_mul_f32 v[112:113], v[4:5], v[112:113] op_sel_hi:[0,1]
	v_pk_mul_f32 v[110:111], v[4:5], v[110:111] op_sel_hi:[0,1]
	v_pk_mul_f32 v[108:109], v[4:5], v[108:109] op_sel_hi:[0,1]
	v_pk_mul_f32 v[106:107], v[4:5], v[106:107] op_sel_hi:[0,1]
	v_pk_mul_f32 v[104:105], v[4:5], v[104:105] op_sel_hi:[0,1]
	v_pk_mul_f32 v[102:103], v[4:5], v[102:103] op_sel_hi:[0,1]
	v_pk_mul_f32 v[100:101], v[4:5], v[100:101] op_sel_hi:[0,1]
	v_pk_mul_f32 v[98:99], v[4:5], v[98:99] op_sel_hi:[0,1]
	s_setprio 1
	v_sub_f32_e32 v1, v1, v10
	v_cmp_le_f32_e32 vcc, s56, v1
	s_cbranch_vccz .LBB1_86
	ds_read_b128 v[114:117], v206 offset:57344
	v_sub_f32_e32 v1, v66, v10
	v_sub_f32_e32 v3, v68, v10
	v_sub_f32_e32 v5, v70, v10
	v_sub_f32_e32 v7, v72, v10
	v_exp_f32_e32 v17, v1
	v_sub_f32_e32 v1, v67, v10
	v_exp_f32_e32 v4, v3
	v_sub_f32_e32 v3, v69, v10
	v_exp_f32_e32 v6, v5
	v_sub_f32_e32 v5, v71, v10
	v_exp_f32_e32 v8, v7
	v_sub_f32_e32 v7, v73, v10
	v_exp_f32_e32 v7, v7
	v_exp_f32_e32 v5, v5
	v_exp_f32_e32 v3, v3
	v_exp_f32_e32 v1, v1
	v_cvt_pk_f16_f32 v239, v8, v7
	v_cvt_pk_f16_f32 v238, v6, v5
	v_cvt_pk_f16_f32 v237, v4, v3
	v_cvt_pk_f16_f32 v236, v17, v1
	s_waitcnt lgkmcnt(0)
	s_nop 0
	v_mfma_f32_32x32x16_f16 v[98:113], v[114:117], v[236:239], v[98:113]
	v_mfma_f32_32x32x16_f16 v[82:97], v[194:197], v[236:239], v[82:97]
	v_sub_f32_e32 v1, v16, v10
	v_cmp_le_f32_e32 vcc, s56, v1
	s_cbranch_vccz .LBB1_50
.LBB1_49:
	v_sub_f32_e32 v4, v76, v10
	v_exp_f32_e32 v8, v4
	v_sub_f32_e32 v4, v78, v10
	v_exp_f32_e32 v17, v4
	v_sub_f32_e32 v4, v80, v10
	v_exp_f32_e32 v115, v4
	ds_read_b128 v[4:7], v206 offset:58368
	v_sub_f32_e32 v1, v74, v10
	v_sub_f32_e32 v3, v75, v10
	v_sub_f32_e32 v16, v77, v10
	v_sub_f32_e32 v114, v79, v10
	v_sub_f32_e32 v116, v81, v10
	v_exp_f32_e32 v1, v1
	v_exp_f32_e32 v116, v116
	v_exp_f32_e32 v114, v114
	v_exp_f32_e32 v16, v16
	v_exp_f32_e32 v3, v3
	v_cvt_pk_f16_f32 v117, v115, v116
	v_cvt_pk_f16_f32 v116, v17, v114
	v_cvt_pk_f16_f32 v115, v8, v16
	v_cvt_pk_f16_f32 v114, v1, v3
	s_waitcnt lgkmcnt(0)
	s_nop 0
	v_mfma_f32_32x32x16_f16 v[98:113], v[4:7], v[114:117], v[98:113]
	v_mfma_f32_32x32x16_f16 v[82:97], v[194:197], v[114:117], v[82:97]
.LBB1_50:
	v_sub_f32_e32 v1, v15, v10
	v_cmp_le_f32_e32 vcc, s56, v1
	s_cbranch_vccz .LBB1_87
	ds_read_b128 v[114:117], v206 offset:59392
	v_sub_f32_e32 v1, v50, v10
	v_sub_f32_e32 v3, v52, v10
	v_sub_f32_e32 v5, v54, v10
	v_sub_f32_e32 v7, v56, v10
	v_exp_f32_e32 v15, v1
	v_sub_f32_e32 v1, v51, v10
	v_exp_f32_e32 v4, v3
	v_sub_f32_e32 v3, v53, v10
	v_exp_f32_e32 v6, v5
	v_sub_f32_e32 v5, v55, v10
	v_exp_f32_e32 v8, v7
	v_sub_f32_e32 v7, v57, v10
	v_exp_f32_e32 v7, v7
	v_exp_f32_e32 v5, v5
	v_exp_f32_e32 v3, v3
	v_exp_f32_e32 v1, v1
	v_cvt_pk_f16_f32 v239, v8, v7
	v_cvt_pk_f16_f32 v238, v6, v5
	v_cvt_pk_f16_f32 v237, v4, v3
	v_cvt_pk_f16_f32 v236, v15, v1
	s_waitcnt lgkmcnt(0)
	s_nop 0
	v_mfma_f32_32x32x16_f16 v[98:113], v[114:117], v[236:239], v[98:113]
	v_mfma_f32_32x32x16_f16 v[82:97], v[194:197], v[236:239], v[82:97]
	v_sub_f32_e32 v1, v14, v10
	v_cmp_le_f32_e32 vcc, s56, v1
	s_cbranch_vccz .LBB1_53
.LBB1_52:
	v_sub_f32_e32 v4, v60, v10
	v_exp_f32_e32 v8, v4
	v_sub_f32_e32 v4, v62, v10
	v_exp_f32_e32 v15, v4
	v_sub_f32_e32 v4, v64, v10
	v_exp_f32_e32 v17, v4
	ds_read_b128 v[4:7], v206 offset:60416
	v_sub_f32_e32 v1, v58, v10
	v_sub_f32_e32 v3, v59, v10
	v_sub_f32_e32 v14, v61, v10
	v_sub_f32_e32 v16, v63, v10
	v_sub_f32_e32 v114, v65, v10
	v_exp_f32_e32 v1, v1
	v_exp_f32_e32 v114, v114
	v_exp_f32_e32 v16, v16
	v_exp_f32_e32 v14, v14
	v_exp_f32_e32 v3, v3
	v_cvt_pk_f16_f32 v17, v17, v114
	v_cvt_pk_f16_f32 v16, v15, v16
	v_cvt_pk_f16_f32 v15, v8, v14
	v_cvt_pk_f16_f32 v14, v1, v3
	s_waitcnt lgkmcnt(0)
	s_nop 0
	v_mfma_f32_32x32x16_f16 v[98:113], v[4:7], v[14:17], v[98:113]
	v_mfma_f32_32x32x16_f16 v[82:97], v[194:197], v[14:17], v[82:97]
.LBB1_53:
	v_sub_f32_e32 v1, v13, v10
	v_cmp_le_f32_e32 vcc, s56, v1
	s_cbranch_vccz .LBB1_88
	ds_read_b128 v[14:17], v206 offset:61440
	v_sub_f32_e32 v1, v34, v10
	v_sub_f32_e32 v3, v36, v10
	v_sub_f32_e32 v5, v38, v10
	v_sub_f32_e32 v7, v40, v10
	v_exp_f32_e32 v13, v1
	v_sub_f32_e32 v1, v35, v10
	v_exp_f32_e32 v4, v3
	v_sub_f32_e32 v3, v37, v10
	v_exp_f32_e32 v6, v5
	v_sub_f32_e32 v5, v39, v10
	v_exp_f32_e32 v8, v7
	v_sub_f32_e32 v7, v41, v10
	v_exp_f32_e32 v7, v7
	v_exp_f32_e32 v5, v5
	v_exp_f32_e32 v3, v3
	v_exp_f32_e32 v1, v1
	v_cvt_pk_f16_f32 v239, v8, v7
	v_cvt_pk_f16_f32 v238, v6, v5
	v_cvt_pk_f16_f32 v237, v4, v3
	v_cvt_pk_f16_f32 v236, v13, v1
	s_waitcnt lgkmcnt(0)
	s_nop 0
	v_mfma_f32_32x32x16_f16 v[98:113], v[14:17], v[236:239], v[98:113]
	v_mfma_f32_32x32x16_f16 v[82:97], v[194:197], v[236:239], v[82:97]
	v_sub_f32_e32 v1, v12, v10
	v_cmp_le_f32_e32 vcc, s56, v1
	s_cbranch_vccz .LBB1_56
.LBB1_55:
	v_sub_f32_e32 v4, v44, v10
	v_exp_f32_e32 v8, v4
	v_sub_f32_e32 v4, v46, v10
	v_exp_f32_e32 v13, v4
	v_sub_f32_e32 v4, v48, v10
	v_exp_f32_e32 v15, v4
	ds_read_b128 v[4:7], v206 offset:62464
	v_sub_f32_e32 v1, v42, v10
	v_sub_f32_e32 v3, v43, v10
	v_sub_f32_e32 v12, v45, v10
	v_sub_f32_e32 v14, v47, v10
	v_sub_f32_e32 v16, v49, v10
	v_exp_f32_e32 v1, v1
	v_exp_f32_e32 v16, v16
	v_exp_f32_e32 v14, v14
	v_exp_f32_e32 v12, v12
	v_exp_f32_e32 v3, v3
	v_cvt_pk_f16_f32 v15, v15, v16
	v_cvt_pk_f16_f32 v14, v13, v14
	v_cvt_pk_f16_f32 v13, v8, v12
	v_cvt_pk_f16_f32 v12, v1, v3
	s_waitcnt lgkmcnt(0)
	s_nop 0
	v_mfma_f32_32x32x16_f16 v[98:113], v[4:7], v[12:15], v[98:113]
	v_mfma_f32_32x32x16_f16 v[82:97], v[194:197], v[12:15], v[82:97]
.LBB1_56:
	v_sub_f32_e32 v1, v11, v10
	v_cmp_le_f32_e32 vcc, s56, v1
	s_cbranch_vccz .LBB1_89
	ds_read_b128 v[12:15], v206 offset:63488
	v_sub_f32_e32 v1, v18, v10
	v_sub_f32_e32 v3, v20, v10
	v_sub_f32_e32 v5, v22, v10
	v_sub_f32_e32 v7, v24, v10
	v_exp_f32_e32 v11, v1
	v_sub_f32_e32 v1, v19, v10
	v_exp_f32_e32 v4, v3
	v_sub_f32_e32 v3, v21, v10
	v_exp_f32_e32 v6, v5
	v_sub_f32_e32 v5, v23, v10
	v_exp_f32_e32 v8, v7
	v_sub_f32_e32 v7, v25, v10
	v_exp_f32_e32 v7, v7
	v_exp_f32_e32 v5, v5
	v_exp_f32_e32 v3, v3
	v_exp_f32_e32 v1, v1
	v_cvt_pk_f16_f32 v239, v8, v7
	v_cvt_pk_f16_f32 v238, v6, v5
	v_cvt_pk_f16_f32 v237, v4, v3
	v_cvt_pk_f16_f32 v236, v11, v1
	s_waitcnt lgkmcnt(0)
	s_nop 0
	v_mfma_f32_32x32x16_f16 v[98:113], v[12:15], v[236:239], v[98:113]
	v_mfma_f32_32x32x16_f16 v[82:97], v[194:197], v[236:239], v[82:97]
	v_sub_f32_e32 v1, v9, v10
	v_cmp_le_f32_e32 vcc, s56, v1
	s_cbranch_vccz .LBB1_59
.LBB1_58:
	v_sub_f32_e32 v4, v28, v10
	v_exp_f32_e32 v8, v4
	v_sub_f32_e32 v4, v30, v10
	v_exp_f32_e32 v12, v4
	v_sub_f32_e32 v4, v32, v10
	v_exp_f32_e32 v13, v4
	ds_read_b128 v[4:7], v206 offset:64512
	v_sub_f32_e32 v1, v26, v10
	v_sub_f32_e32 v3, v27, v10
	v_sub_f32_e32 v9, v29, v10
	v_sub_f32_e32 v11, v31, v10
	v_sub_f32_e32 v10, v33, v10
	v_exp_f32_e32 v1, v1
	v_exp_f32_e32 v10, v10
	v_exp_f32_e32 v14, v11
	v_exp_f32_e32 v9, v9
	v_exp_f32_e32 v3, v3
	v_cvt_pk_f16_f32 v11, v13, v10
	v_cvt_pk_f16_f32 v10, v12, v14
	v_cvt_pk_f16_f32 v9, v8, v9
	v_cvt_pk_f16_f32 v8, v1, v3
	s_waitcnt lgkmcnt(0)
	s_nop 0
	v_mfma_f32_32x32x16_f16 v[98:113], v[4:7], v[8:11], v[98:113]
	v_mfma_f32_32x32x16_f16 v[82:97], v[194:197], v[8:11], v[82:97]

.LBB1_82:
	v_mov_b32_e32 v16, v2
	v_mov_b32_e32 v17, v2
	v_mov_b32_e32 v3, v2
	v_mov_b32_e32 v4, v2
	v_mov_b32_e32 v5, v2
	v_mov_b32_e32 v6, v2
	v_mov_b32_e32 v7, v2
	v_mov_b32_e32 v8, v2
	v_mov_b32_e32 v9, v2
	v_mov_b32_e32 v10, v2
	v_mov_b32_e32 v11, v2
	v_mov_b32_e32 v12, v2
	v_mov_b32_e32 v13, v2
	v_mov_b32_e32 v14, v2
	v_mov_b32_e32 v15, v2
	v_mov_b64_e32 v[112:113], v[16:17]
	v_mov_b64_e32 v[96:97], v[16:17]
	v_mov_b64_e32 v[110:111], v[14:15]
	v_mov_b64_e32 v[108:109], v[12:13]
	v_mov_b64_e32 v[106:107], v[10:11]
	v_mov_b64_e32 v[104:105], v[8:9]
	v_mov_b64_e32 v[102:103], v[6:7]
	v_mov_b64_e32 v[100:101], v[4:5]
	v_mov_b64_e32 v[98:99], v[2:3]
	v_mov_b64_e32 v[94:95], v[14:15]
	v_mov_b64_e32 v[92:93], v[12:13]
	v_mov_b64_e32 v[90:91], v[10:11]
	v_mov_b64_e32 v[88:89], v[8:9]
	v_mov_b64_e32 v[86:87], v[6:7]
	v_mov_b64_e32 v[84:85], v[4:5]
	v_mov_b64_e32 v[82:83], v[2:3]
	v_sub_f32_e32 v1, v243, v236
	v_cmp_le_f32_e32 vcc, s56, v1
	s_cbranch_vccnz .LBB1_22
	s_branch .LBB1_23
.LBB1_83:
	v_sub_f32_e32 v1, v241, v236
	v_cmp_le_f32_e32 vcc, s56, v1
	s_cbranch_vccnz .LBB1_25
	s_branch .LBB1_26
.LBB1_84:
	v_sub_f32_e32 v1, v239, v236
	v_cmp_le_f32_e32 vcc, s56, v1
	s_cbranch_vccnz .LBB1_28
	s_branch .LBB1_29
.LBB1_85:
	v_sub_f32_e32 v1, v237, v236
	v_cmp_le_f32_e32 vcc, s56, v1
	s_cbranch_vccnz .LBB1_31
	s_branch .LBB1_32
.LBB1_86:
	v_sub_f32_e32 v1, v16, v10
	v_cmp_le_f32_e32 vcc, s56, v1
	s_cbranch_vccnz .LBB1_49
	s_branch .LBB1_50
.LBB1_87:
	v_sub_f32_e32 v1, v14, v10
	v_cmp_le_f32_e32 vcc, s56, v1
	s_cbranch_vccnz .LBB1_52
	s_branch .LBB1_53
.LBB1_88:
	v_sub_f32_e32 v1, v12, v10
	v_cmp_le_f32_e32 vcc, s56, v1
	s_cbranch_vccnz .LBB1_55
	s_branch .LBB1_56
.LBB1_89:
	v_sub_f32_e32 v1, v9, v10
	v_cmp_le_f32_e32 vcc, s56, v1
	s_cbranch_vccnz .LBB1_58
	s_branch .LBB1_59
